# v19 + P2: the q/k conv-input rows of PROJ (streamed once) marked nt
# speedup vs baseline: 1.0127x; 1.0023x over previous
; #define GAS __attribute__((address_space(1)))
; DI void m1_item(Frame& F, int hh, int kc) {
;     ...
;         const int chb = (which == 0 ? 1024 : 0) + hh * DH + dg * 8;
;         const int colb = (which == 0 ? C_K : C_Q) + hh * DH + dg * 8;
;         v4u raw[11];
; #pragma unroll
;         for (int rr = 0; rr < 11; ++rr) { const int tt = t0 + sg * 8 - 3 + rr; raw[rr] = (v4u){0u, 0u, 0u, 0u}; if (tt >= 0) raw[rr] = *(const GAS v4u*)(F.PROJ + (size_t)tt * NPROJ + colb); }
.LBB0_432:
	s_and_b64 s[2:3], s[38:39], exec
	s_movk_i32 s2, 0xc00
	s_cselect_b32 s2, s2, 0x800
	v_add_u32_e32 v34, s2, v143
	v_ashrrev_i32_e32 v35, 31, v34
	v_lshl_add_u64 v[50:51], v[34:35], 1, s[66:67]
	v_mov_b32_e32 v72, 0
	v_mov_b32_e32 v68, 0
	v_mov_b32_e32 v69, 0
	v_mov_b32_e32 v70, 0
	v_mov_b32_e32 v71, 0
	s_and_saveexec_b64 s[2:3], s[14:15]
	s_cbranch_execz .LBB0_434
	v_lshl_add_u64 v[34:35], v[50:51], 0, v[144:145]
	global_load_dwordx4 v[68:71], v[34:35], off nt
.LBB0_434:
	s_or_b64 exec, exec, s[2:3]
	v_mov_b32_e32 v73, 0
	v_mov_b32_e32 v74, 0
	v_mov_b32_e32 v75, 0
	s_and_saveexec_b64 s[2:3], s[16:17]
	s_cbranch_execz .LBB0_436
	v_lshl_add_u64 v[34:35], v[50:51], 0, v[152:153]
	global_load_dwordx4 v[72:75], v[34:35], off nt
.LBB0_436:
	s_or_b64 exec, exec, s[2:3]
	v_mov_b32_e32 v84, 0
	v_mov_b32_e32 v88, 0
	v_mov_b32_e32 v89, 0
	v_mov_b32_e32 v90, 0
	v_mov_b32_e32 v91, 0
	s_and_saveexec_b64 s[2:3], s[14:15]
	s_cbranch_execz .LBB0_438
	v_lshl_add_u64 v[34:35], v[50:51], 0, v[154:155]
	global_load_dwordx4 v[88:91], v[34:35], off nt
.LBB0_438:
	s_or_b64 exec, exec, s[2:3]
	v_mov_b32_e32 v85, 0
	v_mov_b32_e32 v86, 0
	v_mov_b32_e32 v87, 0
	s_and_saveexec_b64 s[2:3], s[18:19]
	s_cbranch_execz .LBB0_440
	v_lshl_add_u64 v[34:35], v[50:51], 0, v[156:157]
	global_load_dwordx4 v[84:87], v[34:35], off nt
.LBB0_440:
	s_or_b64 exec, exec, s[2:3]
	v_mov_b32_e32 v60, 0
	v_mov_b32_e32 v76, 0
	v_mov_b32_e32 v77, 0
	v_mov_b32_e32 v78, 0
	v_mov_b32_e32 v79, 0
	s_and_saveexec_b64 s[2:3], s[20:21]
	s_cbranch_execz .LBB0_442
	v_lshl_add_u64 v[34:35], v[50:51], 0, v[158:159]
	global_load_dwordx4 v[76:79], v[34:35], off nt
.LBB0_442:
	s_or_b64 exec, exec, s[2:3]
	v_mov_b32_e32 v61, 0
	v_mov_b32_e32 v62, 0
	v_mov_b32_e32 v63, 0
	s_and_saveexec_b64 s[2:3], s[22:23]
	s_cbranch_execz .LBB0_444
	v_lshl_add_u64 v[34:35], v[50:51], 0, v[160:161]
	global_load_dwordx4 v[60:63], v[34:35], off nt
.LBB0_444:
	s_or_b64 exec, exec, s[2:3]
	v_mov_b32_e32 v46, 0
	v_mov_b32_e32 v52, 0
	v_mov_b32_e32 v53, 0
	v_mov_b32_e32 v54, 0
	v_mov_b32_e32 v55, 0
	s_and_saveexec_b64 s[2:3], s[24:25]
	s_cbranch_execz .LBB0_446
	v_lshl_add_u64 v[34:35], v[50:51], 0, v[162:163]
	global_load_dwordx4 v[52:55], v[34:35], off nt
.LBB0_446:
	s_or_b64 exec, exec, s[2:3]
	v_mov_b32_e32 v47, 0
	v_mov_b32_e32 v48, 0
	v_mov_b32_e32 v49, 0
	s_and_saveexec_b64 s[2:3], s[26:27]
	s_cbranch_execz .LBB0_448
	v_lshl_add_u64 v[34:35], v[50:51], 0, v[164:165]
	global_load_dwordx4 v[46:49], v[34:35], off nt
.LBB0_448:
	s_or_b64 exec, exec, s[2:3]
	v_mov_b32_e32 v38, 0
	v_mov_b32_e32 v42, 0
	v_mov_b32_e32 v43, 0
	v_mov_b32_e32 v44, 0
	v_mov_b32_e32 v45, 0
	s_and_saveexec_b64 s[2:3], s[28:29]
	s_cbranch_execz .LBB0_450
	v_lshl_add_u64 v[34:35], v[50:51], 0, v[166:167]
	global_load_dwordx4 v[42:45], v[34:35], off nt
.LBB0_450:
	s_or_b64 exec, exec, s[2:3]
	v_mov_b32_e32 v39, 0
	v_mov_b32_e32 v40, 0
	v_mov_b32_e32 v41, 0
	s_and_saveexec_b64 s[2:3], s[30:31]
	s_cbranch_execz .LBB0_452
	v_lshl_add_u64 v[34:35], v[50:51], 0, v[168:169]
	global_load_dwordx4 v[38:41], v[34:35], off nt
.LBB0_452:
	s_or_b64 exec, exec, s[2:3]
	v_mov_b32_e32 v34, 0
	v_mov_b32_e32 v35, 0
	v_mov_b32_e32 v36, 0
	v_mov_b32_e32 v37, 0
	s_and_saveexec_b64 s[2:3], s[34:35]
	s_cbranch_execz .LBB0_454
	v_lshl_add_u64 v[34:35], v[50:51], 0, v[170:171]
	global_load_dwordx4 v[34:37], v[34:35], off nt
